# v49 + TLB pre-touch: one 16-lane load per wave touching 16 pages of the batch during the ids-latency window
# baseline (speedup 1.0000x reference)
_Z7vq_mainPKfPKiS0_PfPhPdPi:
	s_load_dwordx4 s[4:7], s[0:1], 0x0
	s_load_dwordx2 s[22:23], s[0:1], 0x10
	s_load_dwordx2 s[20:21], s[0:1], 0x18
	s_load_dwordx4 s[12:15], s[0:1], 0x20
	s_load_dwordx2 s[10:11], s[0:1], 0x30
	s_and_b32 s3, s2, 7
	s_lshl_b32 s3, s3, 6
	s_lshr_b32 s16, s2, 3
	s_add_i32 s16, s16, s3
	s_lshr_b32 s18, s16, 5
	s_mov_b32 s19, 0
	s_and_b32 s28, s16, 31
	s_lshl_b32 s28, s28, 4
	s_add_i32 s29, s28, 1
	v_readfirstlane_b32 s17, v0
	v_and_b32_e32 v1, 63, v0
	v_lshlrev_b32_e32 v66, 4, v0
	s_lshr_b32 s17, s17, 6
	s_lshl_b32 s24, s17, 4
	s_lshl_b32 s30, s18, 15
	s_lshl_b32 s31, s18, 23
	v_add_u32_e32 v67, 0x1000, v66
	v_add_u32_e32 v68, 0x2000, v66
	v_add_u32_e32 v69, 0x3000, v66
	v_add_u32_e32 v70, 0x4000, v66
	v_add_u32_e32 v71, 0x5000, v66
	v_add_u32_e32 v72, 0x6000, v66
	v_add_u32_e32 v73, 0x7000, v66
	s_movk_i32 s9, 0x810
	s_mov_b32 s3, 0x8100
	s_mul_i32 s36, s29, 0x810
	v_mov_b32_e32 v141, s36
	v_sub_u32_e32 v141, 0, v141
	s_waitcnt lgkmcnt(0)
	s_add_u32 s34, s6, s30
	s_addc_u32 s35, s7, 0
	s_add_u32 s32, s4, s31
	s_addc_u32 s33, s5, 0
	global_load_dwordx4 v[74:77], v66, s[34:35]
	global_load_dwordx4 v[78:81], v67, s[34:35]
	global_load_dwordx4 v[82:85], v68, s[34:35]
	global_load_dwordx4 v[86:89], v69, s[34:35]
	global_load_dwordx4 v[90:93], v70, s[34:35]
	global_load_dwordx4 v[94:97], v71, s[34:35]
	global_load_dwordx4 v[98:101], v72, s[34:35]
	global_load_dwordx4 v[102:105], v73, s[34:35]
	v_and_b32_e32 v150, 15, v0
	v_or_b32_e32 v150, s24, v150
	v_and_b32_e32 v151, 48, v0
	v_lshl_or_b32 v150, v150, 10, v151
	global_load_dwordx4 v[62:65], v150, s[22:23] offset:0
	global_load_dwordx4 v[58:61], v150, s[22:23] offset:64
	global_load_dwordx4 v[54:57], v150, s[22:23] offset:128
	global_load_dwordx4 v[50:53], v150, s[22:23] offset:192
	global_load_dwordx4 v[46:49], v150, s[22:23] offset:256
	global_load_dwordx4 v[42:45], v150, s[22:23] offset:320
	global_load_dwordx4 v[38:41], v150, s[22:23] offset:384
	global_load_dwordx4 v[34:37], v150, s[22:23] offset:448
	global_load_dwordx4 v[30:33], v150, s[22:23] offset:512
	global_load_dwordx4 v[26:29], v150, s[22:23] offset:576
	global_load_dwordx4 v[22:25], v150, s[22:23] offset:640
	global_load_dwordx4 v[18:21], v150, s[22:23] offset:704
	global_load_dwordx4 v[14:17], v150, s[22:23] offset:768
	global_load_dwordx4 v[10:13], v150, s[22:23] offset:832
	global_load_dwordx4 v[6:9], v150, s[22:23] offset:896
	global_load_dwordx4 v[2:5], v150, s[22:23] offset:960
	s_lshl_b32 s36, s28, 14
	s_lshl_b32 s37, s17, 16
	s_add_u32 s36, s36, s37
	v_and_b32_e32 v197, 15, v0
	v_lshlrev_b32_e32 v197, 12, v197
	v_add_u32_e32 v197, s36, v197
	s_mov_b64 exec, 0xffff
	global_load_dword v196, v197, s[32:33] nt
	s_mov_b64 exec, -1
	v_mov_b32_e32 v142, 1
	v_mov_b32_e32 v143, 4
	v_mov_b32_e32 v144, 0x11100
	v_lshlrev_b32_e32 v145, 8, v0
	v_lshlrev_b32_e32 v148, 3, v0
	v_mov_b32_e32 v152, 0
	v_mov_b32_e32 v153, 0
	ds_write_b64 v148, v[152:153] offset:32768
	ds_write_b64 v148, v[152:153] offset:34832
	ds_write_b64 v148, v[152:153] offset:36896
	ds_write_b64 v148, v[152:153] offset:38960
	ds_write_b64 v148, v[152:153] offset:41024
	ds_write_b64 v148, v[152:153] offset:43088
	ds_write_b64 v148, v[152:153] offset:45152
	ds_write_b64 v148, v[152:153] offset:47216
	ds_write_b64 v148, v[152:153] offset:49280
	ds_write_b64 v148, v[152:153] offset:51344
	ds_write_b64 v148, v[152:153] offset:53408
	ds_write_b64 v148, v[152:153] offset:55472
	ds_write_b64 v148, v[152:153] offset:57536
	ds_write_b64 v148, v[152:153] offset:59600
	ds_write_b64 v148, v[152:153] offset:61664
	ds_write_b64 v148, v[152:153] offset:63728
	v_cmp_gt_u32_e32 vcc, 16, v0
	s_and_saveexec_b64 s[30:31], vcc
	v_mul_u32_u24_e32 v151, 0x810, v0
	ds_write_b64 v151, v[152:153] offset:34816
	v_mov_b32_e32 v150, 0x11540
	v_mov_b32_e32 v149, 8
	ds_write_b32 v150, v149
	s_mov_b64 exec, s[30:31]
	s_waitcnt lgkmcnt(0)
	s_barrier
	s_waitcnt vmcnt(17)
	v_mad_u32_u24 v74, v74, s9, v141
	v_mad_u32_u24 v75, v75, s9, v141
	v_mad_u32_u24 v76, v76, s9, v141
	v_mad_u32_u24 v77, v77, s9, v141
	v_mad_u32_u24 v78, v78, s9, v141
	v_mad_u32_u24 v79, v79, s9, v141
	v_mad_u32_u24 v80, v80, s9, v141
	v_mad_u32_u24 v81, v81, s9, v141
	v_mad_u32_u24 v82, v82, s9, v141
	v_mad_u32_u24 v83, v83, s9, v141
	v_mad_u32_u24 v84, v84, s9, v141
	v_mad_u32_u24 v85, v85, s9, v141
	v_mad_u32_u24 v86, v86, s9, v141
	v_mad_u32_u24 v87, v87, s9, v141
	v_mad_u32_u24 v88, v88, s9, v141
	v_mad_u32_u24 v89, v89, s9, v141
	v_mad_u32_u24 v90, v90, s9, v141
	v_mad_u32_u24 v91, v91, s9, v141
	v_mad_u32_u24 v92, v92, s9, v141
	v_mad_u32_u24 v93, v93, s9, v141
	v_mad_u32_u24 v94, v94, s9, v141
	v_mad_u32_u24 v95, v95, s9, v141
	v_mad_u32_u24 v96, v96, s9, v141
	v_mad_u32_u24 v97, v97, s9, v141
	v_mad_u32_u24 v98, v98, s9, v141
	v_mad_u32_u24 v99, v99, s9, v141
	v_mad_u32_u24 v100, v100, s9, v141
	v_mad_u32_u24 v101, v101, s9, v141
	v_mad_u32_u24 v102, v102, s9, v141
	v_mad_u32_u24 v103, v103, s9, v141
	v_mad_u32_u24 v104, v104, s9, v141
	v_mad_u32_u24 v105, v105, s9, v141
	v_cmp_gt_u32_e64 s[36:37], s3, v74
	v_cmp_gt_u32_e64 s[38:39], s3, v75
	v_cmp_gt_u32_e64 s[40:41], s3, v76
	v_cmp_gt_u32_e64 s[42:43], s3, v77
	v_cmp_gt_u32_e64 s[44:45], s3, v78
	v_cmp_gt_u32_e64 s[46:47], s3, v79
	v_cmp_gt_u32_e64 s[48:49], s3, v80
	v_cmp_gt_u32_e64 s[50:51], s3, v81
	v_cmp_gt_u32_e64 s[52:53], s3, v82
	v_cmp_gt_u32_e64 s[54:55], s3, v83
	v_cmp_gt_u32_e64 s[56:57], s3, v84
	v_cmp_gt_u32_e64 s[58:59], s3, v85
	v_cmp_gt_u32_e64 s[60:61], s3, v86
	v_cmp_gt_u32_e64 s[62:63], s3, v87
	v_cmp_gt_u32_e64 s[64:65], s3, v88
	v_cmp_gt_u32_e64 s[66:67], s3, v89
	v_cmp_gt_u32_e64 s[68:69], s3, v90
	v_cmp_gt_u32_e64 s[70:71], s3, v91
	v_cmp_gt_u32_e64 s[72:73], s3, v92
	v_cmp_gt_u32_e64 s[74:75], s3, v93
	v_cmp_gt_u32_e64 s[76:77], s3, v94
	v_cmp_gt_u32_e64 s[78:79], s3, v95
	v_cmp_gt_u32_e64 s[80:81], s3, v96
	v_cmp_gt_u32_e64 s[82:83], s3, v97
	v_cmp_gt_u32_e64 s[84:85], s3, v98
	v_cmp_gt_u32_e64 s[86:87], s3, v99
	v_cmp_gt_u32_e64 s[88:89], s3, v100
	v_cmp_gt_u32_e64 s[90:91], s3, v101
	v_cmp_gt_u32_e64 s[92:93], s3, v102
	v_cmp_gt_u32_e64 s[94:95], s3, v103
	v_cmp_gt_u32_e64 s[96:97], s3, v104
	v_cmp_gt_u32_e64 s[98:99], s3, v105
	s_mov_b64 exec, s[36:37]
	ds_add_u32 v74, v142 offset:34816
	s_mov_b64 exec, s[38:39]
	ds_add_u32 v75, v142 offset:34816
	s_mov_b64 exec, s[40:41]
	ds_add_u32 v76, v142 offset:34816
	s_mov_b64 exec, s[42:43]
	ds_add_u32 v77, v142 offset:34816
	s_mov_b64 exec, s[44:45]
	ds_add_u32 v78, v142 offset:34816
	s_mov_b64 exec, s[46:47]
	ds_add_u32 v79, v142 offset:34816
	s_mov_b64 exec, s[48:49]
	ds_add_u32 v80, v142 offset:34816
	s_mov_b64 exec, s[50:51]
	ds_add_u32 v81, v142 offset:34816
	s_mov_b64 exec, s[52:53]
	ds_add_u32 v82, v142 offset:34816
	s_mov_b64 exec, s[54:55]
	ds_add_u32 v83, v142 offset:34816
	s_mov_b64 exec, s[56:57]
	ds_add_u32 v84, v142 offset:34816
	s_mov_b64 exec, s[58:59]
	ds_add_u32 v85, v142 offset:34816
	s_mov_b64 exec, s[60:61]
	ds_add_u32 v86, v142 offset:34816
	s_mov_b64 exec, s[62:63]
	ds_add_u32 v87, v142 offset:34816
	s_mov_b64 exec, s[64:65]
	ds_add_u32 v88, v142 offset:34816
	s_mov_b64 exec, s[66:67]
	ds_add_u32 v89, v142 offset:34816
	s_mov_b64 exec, s[68:69]
	ds_add_u32 v90, v142 offset:34816
	s_mov_b64 exec, s[70:71]
	ds_add_u32 v91, v142 offset:34816
	s_mov_b64 exec, s[72:73]
	ds_add_u32 v92, v142 offset:34816
	s_mov_b64 exec, s[74:75]
	ds_add_u32 v93, v142 offset:34816
	s_mov_b64 exec, s[76:77]
	ds_add_u32 v94, v142 offset:34816
	s_mov_b64 exec, s[78:79]
	ds_add_u32 v95, v142 offset:34816
	s_mov_b64 exec, s[80:81]
	ds_add_u32 v96, v142 offset:34816
	s_mov_b64 exec, s[82:83]
	ds_add_u32 v97, v142 offset:34816
	s_mov_b64 exec, s[84:85]
	ds_add_u32 v98, v142 offset:34816
	s_mov_b64 exec, s[86:87]
	ds_add_u32 v99, v142 offset:34816
	s_mov_b64 exec, s[88:89]
	ds_add_u32 v100, v142 offset:34816
	s_mov_b64 exec, s[90:91]
	ds_add_u32 v101, v142 offset:34816
	s_mov_b64 exec, s[92:93]
	ds_add_u32 v102, v142 offset:34816
	s_mov_b64 exec, s[94:95]
	ds_add_u32 v103, v142 offset:34816
	s_mov_b64 exec, s[96:97]
	ds_add_u32 v104, v142 offset:34816
	s_mov_b64 exec, s[98:99]
	ds_add_u32 v105, v142 offset:34816
	s_mov_b64 exec, -1
	s_waitcnt lgkmcnt(0)
	s_barrier
	v_and_b32_e32 v67, 15, v0
	v_mul_u32_u24_e32 v67, 0x810, v67
	ds_read_b32 v68, v67 offset:34816
	s_waitcnt lgkmcnt(0)
	v_mov_b32_e32 v69, v68
	s_nop 1
	v_add_u32_dpp v69, v69, v69 row_shr:1 row_mask:0xf bank_mask:0xf bound_ctrl:1
	s_nop 1
	v_add_u32_dpp v69, v69, v69 row_shr:2 row_mask:0xf bank_mask:0xf bound_ctrl:1
	s_nop 1
	v_add_u32_dpp v69, v69, v69 row_shr:4 row_mask:0xf bank_mask:0xf bound_ctrl:1
	s_nop 1
	v_add_u32_dpp v69, v69, v69 row_shr:8 row_mask:0xf bank_mask:0xf bound_ctrl:1
	s_nop 1
	v_sub_u32_e32 v70, v69, v68
	v_lshlrev_b32_e32 v70, 2, v70
	v_readlane_b32 s8, v69, 15
	s_cmp_lg_u32 s17, 0
	s_cbranch_scc1 .Lfront_nocursor
	v_cmp_gt_u32_e32 vcc, 16, v1
	s_and_saveexec_b64 s[30:31], vcc
	ds_write_b32 v67, v70 offset:34820
	s_mov_b64 exec, s[30:31]
